# v78 plus nt on the 16 residual-stream (XA) stores of the attention out-projection epilogue (next read about 100 us later)
# baseline (speedup 1.0000x reference)
; __device__ __forceinline__ u32x4 pk8(const f32x4 a, const f32x4 b) { u32x4 q; q.x = cvt_pk_bf16(a[0], a[1]); q.y = cvt_pk_bf16(a[2], a[3]); q.z = cvt_pk_bf16(b[0], b[1]); q.w = cvt_pk_bf16(b[2], b[3]); return q; }
;     __device__ __forceinline__ void fused(f32x4 (&acc)[2][2][4][2], const Unit& u, int wr, int wc, int fr, int fq, PG8_LAS unsigned char* lds, int wid, int lane) const {
;     ...
;           bf16_t* op = out + (size_t)row0 * ldc + col0;
;           if constexpr (XF32) {
;               const float* xp = (const float*)xin + (size_t)row0 * ldc + col0; f32x4 xv[4][2][2];
; #pragma unroll
;               for (int ai = 0; ai < 2; ++ai) {
; #pragma unroll
;                   for (int m = 0; m < 4; ++m)
; #pragma unroll
;                       for (int bj = 0; bj < 2; ++bj)
; #pragma unroll
;                           for (int n = 0; n < 2; ++n) xv[m][bj][n] = *(const f32x4*)(xp + (size_t)(ai * HALF + m * 16) * ldc + bj * HALF + n * 4);
; #pragma unroll
;                   for (int m = 0; m < 4; ++m)
; #pragma unroll
;                       for (int bj = 0; bj < 2; ++bj) { acc[ai][bj][m][0] = xv[m][bj][0] + gv[bj][0] * acc[ai][bj][m][0]; acc[ai][bj][m][1] = xv[m][bj][1] + gv[bj][1] * acc[ai][bj][m][1];
;                           *(u32x4*)(op + (size_t)(ai * HALF + m * 16) * ldc + bj * HALF) = pk8(acc[ai][bj][m][0], acc[ai][bj][m][1]); }
.LBB0_666:
	s_lshl_b32 s6, s36, 5
	v_ashrrev_i32_e32 v128, 1, v187
	s_lshl_b32 s7, s4, 8
	v_and_b32_e32 v128, -8, v128
	s_or_b32 s6, s7, s6
	s_ashr_i32 s8, s3, 31
	v_add_u32_e32 v144, s6, v128
	s_lshr_b32 s6, s8, 20
	s_add_i32 s6, s3, s6
	s_ashr_i32 s6, s6, 12
	v_ashrrev_i32_e32 v145, 31, v144
	v_mov_b32_e32 v128, 0x1800
	v_mad_i64_i32 v[128:129], s[6:7], s6, v128, v[144:145]
	v_lshl_add_u64 v[172:173], v[128:129], 2, s[78:79]
	s_mov_b32 s9, 0x102000
	v_add_co_u32_e32 v128, vcc, s9, v172
	v_add_u32_e32 v146, s3, v186
	v_readlane_b32 s44, v254, 36
	v_addc_co_u32_e32 v129, vcc, 0, v173, vcc
	v_ashrrev_i32_e32 v147, 31, v146
	v_readlane_b32 s45, v254, 37
	v_readlane_b32 s48, v254, 40
	v_readlane_b32 s49, v254, 41
	s_barrier
	global_load_dwordx4 v[132:135], v[128:129], off
	v_lshlrev_b64 v[128:129], 12, v[146:147]
	s_mov_b64 s[48:49], s[44:45]
	s_mov_b64 s[6:7], 0x102000
	v_lshl_add_u64 v[128:129], s[48:49], 0, v[128:129]
	v_lshl_add_u64 v[184:185], v[144:145], 2, v[128:129]
	v_lshl_add_u64 v[128:129], v[172:173], 0, s[6:7]
	s_mov_b32 s6, 0x10000
	s_mov_b64 s[10:11], 0x10000
	v_add_co_u32_e32 v164, vcc, s6, v184
	v_lshl_add_u64 v[166:167], v[184:185], 0, s[10:11]
	s_nop 0
	v_addc_co_u32_e32 v165, vcc, 0, v185, vcc
	s_mov_b64 s[10:11], 0x10200
	s_mov_b32 s7, 0x20000
	global_load_dwordx4 v[148:151], v[184:185], off offset:16
	global_load_dwordx4 v[152:155], v[184:185], off
	global_load_dwordx4 v[140:143], v[128:129], off offset:16
	global_load_dwordx4 v[136:139], v[128:129], off offset:512
	global_load_dwordx4 v[156:159], v[184:185], off offset:528
	global_load_dwordx4 v[160:163], v[184:185], off offset:512
	s_nop 0
	global_load_dwordx4 v[128:131], v[128:129], off offset:528
	s_mov_b32 s9, 0x80000
	global_load_dwordx4 v[190:193], v[164:165], off
	global_load_dwordx4 v[194:197], v[166:167], off offset:16
	v_lshl_add_u64 v[166:167], v[184:185], 0, s[10:11]
	global_load_dwordx4 v[198:201], v[164:165], off offset:512
	global_load_dwordx4 v[202:205], v[166:167], off offset:16
	s_mov_b64 s[10:11], 0x20000
	v_add_co_u32_e32 v164, vcc, s7, v184
	v_lshl_add_u64 v[166:167], v[184:185], 0, s[10:11]
	s_nop 0
	v_addc_co_u32_e32 v165, vcc, 0, v185, vcc
	s_mov_b64 s[10:11], 0x20200
	global_load_dwordx4 v[206:209], v[164:165], off
	global_load_dwordx4 v[210:213], v[166:167], off offset:16
	v_lshl_add_u64 v[166:167], v[184:185], 0, s[10:11]
	s_mov_b64 s[10:11], 0x30000
	s_mov_b32 s7, 0x30000
	global_load_dwordx4 v[214:217], v[164:165], off offset:512
	global_load_dwordx4 v[218:221], v[166:167], off offset:16
	v_add_co_u32_e32 v164, vcc, s7, v184
	v_lshl_add_u64 v[166:167], v[184:185], 0, s[10:11]
	s_nop 0
	v_addc_co_u32_e32 v165, vcc, 0, v185, vcc
	global_load_dwordx4 v[226:229], v[166:167], off offset:16
	s_mov_b64 s[10:11], 0x30200
	global_load_dwordx4 v[222:225], v[164:165], off
	global_load_dwordx4 v[230:233], v[164:165], off offset:512
	v_lshl_add_u64 v[164:165], v[184:185], 0, s[10:11]
	global_load_dwordx4 v[234:237], v[164:165], off offset:16
	v_lshlrev_b64 v[166:167], 11, v[146:147]
	v_lshl_add_u64 v[166:167], s[18:19], 0, v[166:167]
	v_lshl_add_u64 v[182:183], v[144:145], 1, v[166:167]
	s_mov_b32 s7, 0x8000
	s_mov_b32 s10, 0xb0000
	s_lshl_b32 s5, s5, 10
	v_readlane_b32 s56, v254, 48
	v_readlane_b32 s57, v254, 49
	v_readlane_b32 s58, v254, 50
	v_readlane_b32 s59, v254, 51
	v_readlane_b32 s52, v254, 44
	v_readlane_b32 s53, v254, 45
	v_readlane_b32 s54, v254, 46
	v_readlane_b32 s55, v254, 47
	s_mov_b64 s[62:63], s[58:59]
	s_mov_b64 s[60:61], s[56:57]
	s_mov_b64 s[58:59], s[54:55]
	v_readlane_b32 s46, v254, 38
	v_readlane_b32 s47, v254, 39
	v_readlane_b32 s50, v254, 42
	v_readlane_b32 s51, v254, 43
	s_mov_b64 s[56:57], s[52:53]
	s_waitcnt vmcnt(0)
	v_pk_fma_f32 v[180:181], v[120:121], v[140:141], v[148:149]
	v_pk_fma_f32 v[174:175], v[126:127], v[134:135], v[154:155]
	v_pk_fma_f32 v[170:171], v[104:105], v[128:129], v[156:157]
	v_pk_fma_f32 v[176:177], v[124:125], v[132:133], v[152:153]
	v_pk_fma_f32 v[178:179], v[122:123], v[142:143], v[150:151]
	v_pk_fma_f32 v[156:157], v[108:109], v[140:141], v[194:195]
	v_add_co_u32_e32 v108, vcc, s7, v182
	v_cvt_pk_bf16_f32 v120, v176, v177
	v_cvt_pk_bf16_f32 v121, v174, v175
	v_cvt_pk_bf16_f32 v122, v180, v181
	v_cvt_pk_bf16_f32 v123, v178, v179
	s_nop 1
	v_addc_co_u32_e32 v109, vcc, 0, v183, vcc
	global_store_dwordx4 v[182:183], v[120:123], off nt
	v_pk_fma_f32 v[164:165], v[118:119], v[138:139], v[162:163]
	v_pk_fma_f32 v[166:167], v[116:117], v[136:137], v[160:161]
	v_pk_fma_f32 v[168:169], v[106:107], v[130:131], v[158:159]
	v_cvt_pk_bf16_f32 v104, v166, v167
	v_cvt_pk_bf16_f32 v105, v164, v165
	v_cvt_pk_bf16_f32 v106, v170, v171
	v_pk_fma_f32 v[120:121], v[92:93], v[140:141], v[210:211]
	v_cvt_pk_bf16_f32 v107, v168, v169
	v_add_co_u32_e32 v92, vcc, s6, v182
	global_store_dwordx4 v[182:183], v[104:107], off offset:256 nt
	v_pk_fma_f32 v[160:161], v[114:115], v[134:135], v[192:193]
	v_pk_fma_f32 v[162:163], v[112:113], v[132:133], v[190:191]
	v_pk_fma_f32 v[158:159], v[110:111], v[142:143], v[196:197]
	v_cvt_pk_bf16_f32 v104, v162, v163
	v_cvt_pk_bf16_f32 v105, v160, v161
	v_cvt_pk_bf16_f32 v106, v156, v157
	v_pk_fma_f32 v[150:151], v[98:99], v[138:139], v[200:201]
	v_cvt_pk_bf16_f32 v107, v158, v159
	global_store_dwordx4 v[108:109], v[104:107], off nt
	v_pk_fma_f32 v[154:155], v[96:97], v[136:137], v[198:199]
	v_pk_fma_f32 v[148:149], v[90:91], v[130:131], v[204:205]
	v_pk_fma_f32 v[152:153], v[88:89], v[128:129], v[202:203]
	v_cvt_pk_bf16_f32 v88, v154, v155
	v_cvt_pk_bf16_f32 v89, v150, v151
	v_addc_co_u32_e32 v93, vcc, 0, v183, vcc
	v_cvt_pk_bf16_f32 v90, v152, v153
	v_cvt_pk_bf16_f32 v91, v148, v149
; __device__ __forceinline__ u32x4 pk8(const f32x4 a, const f32x4 b) { u32x4 q; q.x = cvt_pk_bf16(a[0], a[1]); q.y = cvt_pk_bf16(a[2], a[3]); q.z = cvt_pk_bf16(b[0], b[1]); q.w = cvt_pk_bf16(b[2], b[3]); return q; }
;     __device__ __forceinline__ void fused(f32x4 (&acc)[2][2][4][2], const Unit& u, int wr, int wc, int fr, int fq, PG8_LAS unsigned char* lds, int wid, int lane) const {
;     ...
;                           for (int n = 0; n < 2; ++n) xv[m][bj][n] = *(const f32x4*)(xp + (size_t)(ai * HALF + m * 16) * ldc + bj * HALF + n * 4);
; #pragma unroll
;                   for (int m = 0; m < 4; ++m)
; #pragma unroll
;                       for (int bj = 0; bj < 2; ++bj) { acc[ai][bj][m][0] = xv[m][bj][0] + gv[bj][0] * acc[ai][bj][m][0]; acc[ai][bj][m][1] = xv[m][bj][1] + gv[bj][1] * acc[ai][bj][m][1];
;                           *(u32x4*)(op + (size_t)(ai * HALF + m * 16) * ldc + bj * HALF) = pk8(acc[ai][bj][m][0], acc[ai][bj][m][1]); }
;                   asm volatile("" ::: "memory"); }
	s_mov_b32 s6, 0x18000
	global_store_dwordx4 v[108:109], v[88:91], off offset:256 nt
	v_pk_fma_f32 v[124:125], v[102:103], v[134:135], v[208:209]
	v_pk_fma_f32 v[126:127], v[100:101], v[132:133], v[206:207]
	v_pk_fma_f32 v[122:123], v[94:95], v[142:143], v[212:213]
	v_cvt_pk_bf16_f32 v88, v126, v127
	v_cvt_pk_bf16_f32 v89, v124, v125
	v_cvt_pk_bf16_f32 v90, v120, v121
	v_pk_fma_f32 v[118:119], v[80:81], v[136:137], v[214:215]
	v_cvt_pk_bf16_f32 v91, v122, v123
	global_store_dwordx4 v[92:93], v[88:91], off nt
	v_pk_fma_f32 v[116:117], v[72:73], v[128:129], v[218:219]
	v_cvt_pk_bf16_f32 v72, v118, v119
	v_pk_fma_f32 v[104:105], v[76:77], v[140:141], v[226:227]
	v_add_co_u32_e32 v76, vcc, s6, v182
	v_pk_fma_f32 v[114:115], v[82:83], v[138:139], v[216:217]
	v_pk_fma_f32 v[112:113], v[74:75], v[130:131], v[220:221]
	v_cvt_pk_bf16_f32 v73, v114, v115
	v_cvt_pk_bf16_f32 v74, v116, v117
	v_pk_fma_f32 v[110:111], v[84:85], v[132:133], v[222:223]
	v_cvt_pk_bf16_f32 v75, v112, v113
	global_store_dwordx4 v[92:93], v[72:75], off offset:256 nt
	v_addc_co_u32_e32 v77, vcc, 0, v183, vcc
	s_nop 0
	v_cvt_pk_bf16_f32 v72, v110, v111
	v_pk_fma_f32 v[108:109], v[86:87], v[134:135], v[224:225]
	v_pk_fma_f32 v[106:107], v[78:79], v[142:143], v[228:229]
	v_cvt_pk_bf16_f32 v73, v108, v109
	v_cvt_pk_bf16_f32 v74, v104, v105
	v_pk_fma_f32 v[90:91], v[70:71], v[138:139], v[232:233]
	v_cvt_pk_bf16_f32 v75, v106, v107
	global_store_dwordx4 v[76:77], v[72:75], off nt
	v_pk_fma_f32 v[94:95], v[68:69], v[136:137], v[230:231]
	v_pk_fma_f32 v[88:89], v[66:67], v[130:131], v[236:237]
	v_pk_fma_f32 v[92:93], v[64:65], v[128:129], v[234:235]
	v_cvt_pk_bf16_f32 v64, v94, v95
	v_cvt_pk_bf16_f32 v65, v90, v91
	s_mov_b64 s[6:7], 0x80000
	v_cvt_pk_bf16_f32 v66, v92, v93
	v_cvt_pk_bf16_f32 v67, v88, v89
	global_store_dwordx4 v[76:77], v[64:67], off offset:256 nt
	v_add_co_u32_e32 v72, vcc, s9, v184
	v_lshl_add_u64 v[68:69], v[184:185], 0, s[6:7]
	s_nop 0
	v_addc_co_u32_e32 v73, vcc, 0, v185, vcc
	s_mov_b64 s[6:7], 0x80200
	s_mov_b32 s9, 0x90000
	global_load_dwordx4 v[64:67], v[72:73], off
	v_lshl_add_u64 v[76:77], v[184:185], 0, s[6:7]
	s_mov_b64 s[6:7], 0x90000
	v_add_co_u32_e32 v80, vcc, s9, v184
	v_lshl_add_u64 v[82:83], v[184:185], 0, s[6:7]
	s_nop 0
	v_addc_co_u32_e32 v81, vcc, 0, v185, vcc
	s_mov_b64 s[6:7], 0x90200
	s_mov_b32 s9, 0xa0000
	global_load_dwordx4 v[68:71], v[68:69], off offset:16
	s_nop 0
	global_load_dwordx4 v[72:75], v[72:73], off offset:512
	s_nop 0
	global_load_dwordx4 v[76:79], v[76:77], off offset:16
	s_waitcnt vmcnt(3)
	v_pk_fma_f32 v[102:103], v[60:61], v[132:133], v[64:65]
	global_load_dwordx4 v[190:193], v[80:81], off
	global_load_dwordx4 v[194:197], v[82:83], off offset:16
	v_lshl_add_u64 v[82:83], v[184:185], 0, s[6:7]
	global_load_dwordx4 v[198:201], v[80:81], off offset:512
	global_load_dwordx4 v[202:205], v[82:83], off offset:16
	s_mov_b64 s[6:7], 0xa0000
	v_add_co_u32_e32 v80, vcc, s9, v184
	v_lshl_add_u64 v[82:83], v[184:185], 0, s[6:7]
	s_nop 0
	v_addc_co_u32_e32 v81, vcc, 0, v185, vcc
	s_mov_b64 s[6:7], 0xa0200
	global_load_dwordx4 v[206:209], v[80:81], off
	global_load_dwordx4 v[210:213], v[82:83], off offset:16
	v_lshl_add_u64 v[82:83], v[184:185], 0, s[6:7]
	global_load_dwordx4 v[214:217], v[80:81], off offset:512
	global_load_dwordx4 v[218:221], v[82:83], off offset:16
	s_mov_b64 s[6:7], 0xb0000
	v_add_co_u32_e32 v80, vcc, s10, v184
	s_lshl_b32 s9, s36, 2
	s_nop 0
	v_addc_co_u32_e32 v81, vcc, 0, v185, vcc
	v_lshl_add_u64 v[82:83], v[184:185], 0, s[6:7]
	global_load_dwordx4 v[222:225], v[80:81], off
	global_load_dwordx4 v[226:229], v[82:83], off offset:16
	s_add_i32 s6, s9, 0
	s_add_i32 s5, s6, s5
	s_mov_b64 s[6:7], 0xb0200
	v_lshl_add_u64 v[82:83], v[184:185], 0, s[6:7]
	global_load_dwordx4 v[230:233], v[80:81], off offset:512
	global_load_dwordx4 v[234:237], v[82:83], off offset:16
	s_mov_b32 s6, 0x40000
	v_add_co_u32_e32 v60, vcc, s6, v182
	s_mov_b32 s6, 0x48000
	s_nop 0
	v_addc_co_u32_e32 v61, vcc, 0, v183, vcc
	s_waitcnt vmcnt(13)
	v_pk_fma_f32 v[86:87], v[48:49], v[136:137], v[72:73]
	v_pk_fma_f32 v[100:101], v[62:63], v[134:135], v[66:67]
	v_pk_fma_f32 v[96:97], v[56:57], v[140:141], v[68:69]
	v_cvt_pk_bf16_f32 v56, v102, v103
	v_cvt_pk_bf16_f32 v57, v100, v101
	v_pk_fma_f32 v[98:99], v[58:59], v[142:143], v[70:71]
	v_cvt_pk_bf16_f32 v58, v96, v97
	v_pk_fma_f32 v[82:83], v[50:51], v[138:139], v[74:75]
	v_cvt_pk_bf16_f32 v59, v98, v99
	global_store_dwordx4 v[60:61], v[56:59], off nt
	s_waitcnt vmcnt(13)
; __device__ __forceinline__ u32x4 pk8(const f32x4 a, const f32x4 b) { u32x4 q; q.x = cvt_pk_bf16(a[0], a[1]); q.y = cvt_pk_bf16(a[2], a[3]); q.z = cvt_pk_bf16(b[0], b[1]); q.w = cvt_pk_bf16(b[2], b[3]); return q; }
;     __device__ __forceinline__ bool run(const f32x4 (&v)[2][2][4][2], const Unit& u, int wr, int wc, int fr, int fq, PG8_LAS unsigned char* lds, int wid, int lane) const {
;     ...
;             for (int m = 0; m < 4; ++m) { float s = 0.f;
; #pragma unroll
;                 for (int bj = 0; bj < 2; ++bj)
; #pragma unroll
;                     for (int n = 0; n < 2; ++n) { const f32x4 x = v[ai][bj][m][n]; s += (x[0] * x[0] + x[1] * x[1]) + (x[2] * x[2] + x[3] * x[3]); }
;                 s += __shfl_xor(s, 16); s += __shfl_xor(s, 32);
;                 if (fq == 0) P[(ai * HALF + wr * 64 + m * 16 + fr) * 4 + wc] = s; }
;     __device__ __forceinline__ void fused(f32x4 (&acc)[2][2][4][2], const Unit& u, int wr, int wc, int fr, int fq, PG8_LAS unsigned char* lds, int wid, int lane) const {
;     ...
;                       for (int bj = 0; bj < 2; ++bj) { acc[ai][bj][m][0] = xv[m][bj][0] + gv[bj][0] * acc[ai][bj][m][0]; acc[ai][bj][m][1] = xv[m][bj][1] + gv[bj][1] * acc[ai][bj][m][1];
;                           *(u32x4*)(op + (size_t)(ai * HALF + m * 16) * ldc + bj * HALF) = pk8(acc[ai][bj][m][0], acc[ai][bj][m][1]); }
	v_pk_fma_f32 v[84:85], v[40:41], v[128:129], v[76:77]
	v_cvt_pk_bf16_f32 v40, v86, v87
	v_cvt_pk_bf16_f32 v41, v82, v83
	v_pk_fma_f32 v[80:81], v[42:43], v[130:131], v[78:79]
	v_cvt_pk_bf16_f32 v42, v84, v85
	s_waitcnt vmcnt(12)
	v_pk_fma_f32 v[76:77], v[54:55], v[134:135], v[192:193]
	s_waitcnt vmcnt(11)
	v_pk_fma_f32 v[72:73], v[44:45], v[140:141], v[194:195]
	v_add_co_u32_e32 v44, vcc, s6, v182
	s_mov_b32 s6, 0x50000
	s_nop 0
	v_addc_co_u32_e32 v45, vcc, 0, v183, vcc
	v_cvt_pk_bf16_f32 v43, v80, v81
	global_store_dwordx4 v[60:61], v[40:43], off offset:256 nt
	v_pk_fma_f32 v[78:79], v[52:53], v[132:133], v[190:191]
	v_pk_fma_f32 v[74:75], v[46:47], v[142:143], v[196:197]
	v_cvt_pk_bf16_f32 v40, v78, v79
	s_waitcnt vmcnt(8)
	v_pk_fma_f32 v[56:57], v[28:29], v[140:141], v[210:211]
	v_add_co_u32_e32 v28, vcc, s6, v182
	v_cvt_pk_bf16_f32 v41, v76, v77
	s_mov_b32 s6, 0x58000
	s_nop 0
	v_addc_co_u32_e32 v29, vcc, 0, v183, vcc
	v_cvt_pk_bf16_f32 v42, v72, v73
	v_cvt_pk_bf16_f32 v43, v74, v75
	global_store_dwordx4 v[44:45], v[40:43], off nt
	v_pk_fma_f32 v[66:67], v[34:35], v[138:139], v[200:201]
	v_pk_fma_f32 v[70:71], v[32:33], v[136:137], v[198:199]
	v_pk_fma_f32 v[64:65], v[26:27], v[130:131], v[204:205]
	v_pk_fma_f32 v[68:69], v[24:25], v[128:129], v[202:203]
	v_cvt_pk_bf16_f32 v24, v70, v71
	v_cvt_pk_bf16_f32 v25, v66, v67
	s_waitcnt vmcnt(5)
	v_pk_fma_f32 v[40:41], v[12:13], v[140:141], v[226:227]
	v_cvt_pk_bf16_f32 v26, v68, v69
	v_cvt_pk_bf16_f32 v27, v64, v65
	v_add_co_u32_e32 v12, vcc, s6, v182
	global_store_dwordx4 v[44:45], v[24:27], off offset:256 nt
	v_pk_fma_f32 v[60:61], v[38:39], v[134:135], v[208:209]
	v_pk_fma_f32 v[62:63], v[36:37], v[132:133], v[206:207]
	v_pk_fma_f32 v[58:59], v[30:31], v[142:143], v[212:213]
	v_cvt_pk_bf16_f32 v24, v62, v63
	v_cvt_pk_bf16_f32 v25, v60, v61
	v_cvt_pk_bf16_f32 v26, v56, v57
	v_pk_fma_f32 v[50:51], v[18:19], v[138:139], v[216:217]
	v_cvt_pk_bf16_f32 v27, v58, v59
	global_store_dwordx4 v[28:29], v[24:27], off nt
	v_pk_fma_f32 v[54:55], v[16:17], v[136:137], v[214:215]
	v_pk_fma_f32 v[48:49], v[10:11], v[130:131], v[220:221]
	v_pk_fma_f32 v[52:53], v[8:9], v[128:129], v[218:219]
	v_cvt_pk_bf16_f32 v8, v54, v55
	v_cvt_pk_bf16_f32 v9, v50, v51
	v_addc_co_u32_e32 v13, vcc, 0, v183, vcc
	v_cvt_pk_bf16_f32 v10, v52, v53
	v_cvt_pk_bf16_f32 v11, v48, v49
	global_store_dwordx4 v[28:29], v[8:11], off offset:256 nt
	v_pk_fma_f32 v[44:45], v[22:23], v[134:135], v[224:225]
	v_pk_fma_f32 v[46:47], v[20:21], v[132:133], v[222:223]
	v_pk_fma_f32 v[42:43], v[14:15], v[142:143], v[228:229]
	v_cvt_pk_bf16_f32 v8, v46, v47
	v_cvt_pk_bf16_f32 v9, v44, v45
	v_cvt_pk_bf16_f32 v10, v40, v41
	s_waitcnt vmcnt(7)
	v_pk_fma_f32 v[34:35], v[6:7], v[138:139], v[232:233]
	v_cvt_pk_bf16_f32 v11, v42, v43
	global_store_dwordx4 v[12:13], v[8:11], off nt
	v_pk_fma_f32 v[38:39], v[4:5], v[136:137], v[230:231]
	s_waitcnt vmcnt(7)
	v_pk_fma_f32 v[32:33], v[2:3], v[130:131], v[236:237]
	v_pk_fma_f32 v[36:37], v[0:1], v[128:129], v[234:235]
	v_cvt_pk_bf16_f32 v0, v38, v39
	v_cvt_pk_bf16_f32 v1, v34, v35
	v_mul_f32_e32 v4, v175, v175
	v_cvt_pk_bf16_f32 v2, v36, v37
	v_cvt_pk_bf16_f32 v3, v32, v33
	global_store_dwordx4 v[12:13], v[0:3], off offset:256 nt
	v_fmac_f32_e32 v4, v174, v174
	v_mul_f32_e32 v5, v179, v179
	v_mul_f32_e32 v3, v177, v177
	v_fmac_f32_e32 v3, v176, v176
	v_add_f32_e32 v3, v3, v4
	v_mul_f32_e32 v4, v181, v181
	v_fmac_f32_e32 v4, v180, v180
	v_fmac_f32_e32 v5, v178, v178
	v_add_f32_e32 v4, v4, v5
	v_mbcnt_lo_u32_b32 v0, -1, 0
	v_add_f32_e32 v3, v3, v4
	v_mul_f32_e32 v4, v167, v167
	v_mul_f32_e32 v5, v165, v165
	v_mbcnt_hi_u32_b32 v1, -1, v0
	v_fmac_f32_e32 v4, v166, v166
	v_fmac_f32_e32 v5, v164, v164
	v_and_b32_e32 v2, 64, v1
	v_add_f32_e32 v4, v4, v5
	v_xor_b32_e32 v0, 16, v1
	v_add_u32_e32 v2, 64, v2
	v_add_f32_e32 v3, v3, v4
	v_mul_f32_e32 v4, v171, v171
	v_mul_f32_e32 v5, v169, v169
	v_cmp_lt_i32_e32 vcc, v0, v2
	v_fmac_f32_e32 v4, v170, v170
	v_fmac_f32_e32 v5, v168, v168
	v_cndmask_b32_e32 v0, v1, v0, vcc
	v_add_f32_e32 v4, v4, v5
	v_lshlrev_b32_e32 v0, 2, v0
	v_add_f32_e32 v3, v3, v4
	v_mov_b32_e32 v4, v3
	s_nop 1
	v_permlane16_swap_b32_e32 v4, v3
	v_xor_b32_e32 v5, 32, v1
	v_cmp_lt_i32_e32 vcc, v5, v2
	s_waitcnt lgkmcnt(0)
	v_add_f32_e32 v3, v3, v4
	v_cndmask_b32_e32 v1, v1, v5, vcc
	v_lshlrev_b32_e32 v2, 2, v1
	v_mov_b32_e32 v4, v3
	s_nop 1
	v_permlane32_swap_b32_e32 v4, v3
	v_cmp_gt_u32_e32 vcc, 16, v187
	v_add_u32_e32 v1, s5, v188
	s_and_saveexec_b64 s[6:7], vcc
	s_cbranch_execz .LBB0_668
	s_waitcnt lgkmcnt(0)
	v_add_f32_e32 v3, v3, v4
	ds_write_b32 v1, v3
